# v20
# speedup vs baseline: 1.0078x; 1.0078x over previous
.LBB0_2:
	s_or_b64 exec, exec, s[4:5]
	v_mov_b32_e32 v3, 0
	v_lshlrev_b32_e32 v130, 2, v0
	v_and_b32_e32 v131, 63, v0
	v_readfirstlane_b32 s3, v0
	v_lshlrev_b32_e32 v204, 4, v131
	v_lshlrev_b32_e32 v222, 4, v0
	v_add_u32_e32 v223, 0x2000, v222
	v_add_u32_e32 v224, 0x4000, v222
	v_add_u32_e32 v225, 0x6000, v222
	v_add_u32_e32 v226, 0x8000, v222
	v_add_u32_e32 v227, 0xa000, v222
	v_add_u32_e32 v228, 0xc000, v222
	v_add_u32_e32 v229, 0xe000, v222
	v_add_u32_e32 v230, 0x10000, v222
	v_add_u32_e32 v231, 0x12000, v222
	v_add_u32_e32 v232, 0x14000, v222
	v_add_u32_e32 v233, 0x16000, v222
	v_add_u32_e32 v234, 0x18000, v222
	v_add_u32_e32 v235, 0x1a000, v222
	v_add_u32_e32 v236, 0x1c000, v222
	v_add_u32_e32 v237, 0x1e000, v222
	s_lshr_b32 s31, s3, 6
	s_lshl_b32 s33, s2, 21
	s_waitcnt lgkmcnt(0)
	s_mov_b64 s[40:41], s[14:15]
	s_mov_b32 s15, 0x20000
	s_brev_b32 s14, -2
	s_and_b32 s13, s13, 0xffff
	global_load_dwordx4 v[4:7], v222, s[40:41]
	global_load_dwordx4 v[8:11], v223, s[40:41]
	global_load_dwordx4 v[12:15], v224, s[40:41]
	global_load_dwordx4 v[16:19], v225, s[40:41]
	global_load_dwordx4 v[20:23], v226, s[40:41]
	global_load_dwordx4 v[24:27], v227, s[40:41]
	global_load_dwordx4 v[28:31], v228, s[40:41]
	global_load_dwordx4 v[98:101], v229, s[40:41]
	global_load_dwordx4 v[102:105], v230, s[40:41]
	global_load_dwordx4 v[106:109], v231, s[40:41]
	global_load_dwordx4 v[110:113], v232, s[40:41]
	global_load_dwordx4 v[114:117], v233, s[40:41]
	global_load_dwordx4 v[118:121], v234, s[40:41]
	global_load_dwordx4 v[122:125], v235, s[40:41]
	global_load_dwordx4 v[126:129], v236, s[40:41]
	global_load_dwordx4 v[132:135], v237, s[40:41]
	s_load_dwordx2 s[20:21], s[0:1], 0x50
	s_load_dwordx2 s[22:23], s[0:1], 0x40
	s_load_dwordx2 s[4:5], s[0:1], 0x20
	s_load_dwordx4 s[16:19], s[0:1], 0x30
	s_lshl_b32 s6, s31, 14
	s_add_i32 s6, s6, s33
	s_or_b32 s7, s6, 0x1000
	buffer_load_dwordx4 v[34:37], v204, s[12:15], s6 offen sc0 nt sc1
	buffer_load_dwordx4 v[38:41], v204, s[12:15], s7 offen sc0 nt sc1
	s_or_b32 s7, s6, 0x2000
	s_or_b32 s8, s6, 0x3000
	buffer_load_dwordx4 v[42:45], v204, s[12:15], s7 offen sc0 nt sc1
	buffer_load_dwordx4 v[46:49], v204, s[12:15], s8 offen sc0 nt sc1
	s_or_b32 s7, s6, 0x400
	s_or_b32 s8, s6, 0x1400
	buffer_load_dwordx4 v[50:53], v204, s[12:15], s7 offen sc0 nt sc1
	buffer_load_dwordx4 v[54:57], v204, s[12:15], s8 offen sc0 nt sc1
	s_or_b32 s7, s6, 0x2400
	s_or_b32 s8, s6, 0x3400
	buffer_load_dwordx4 v[58:61], v204, s[12:15], s7 offen sc0 nt sc1
	buffer_load_dwordx4 v[62:65], v204, s[12:15], s8 offen sc0 nt sc1
	s_or_b32 s7, s6, 0x800
	s_or_b32 s8, s6, 0x1800
	buffer_load_dwordx4 v[66:69], v204, s[12:15], s7 offen sc0 nt sc1
	buffer_load_dwordx4 v[70:73], v204, s[12:15], s8 offen sc0 nt sc1
	s_or_b32 s7, s6, 0x2800
	s_or_b32 s8, s6, 0x3800
	buffer_load_dwordx4 v[74:77], v204, s[12:15], s7 offen sc0 nt sc1
	buffer_load_dwordx4 v[78:81], v204, s[12:15], s8 offen sc0 nt sc1
	s_or_b32 s7, s6, 0xc00
	s_or_b32 s8, s6, 0x1c00
	buffer_load_dwordx4 v[82:85], v204, s[12:15], s7 offen sc0 nt sc1
	buffer_load_dwordx4 v[86:89], v204, s[12:15], s8 offen sc0 nt sc1
	s_or_b32 s7, s6, 0x2c00
	s_or_b32 s6, s6, 0x3c00
	buffer_load_dwordx4 v[90:93], v204, s[12:15], s7 offen sc0 nt sc1
	buffer_load_dwordx4 v[94:97], v204, s[12:15], s6 offen sc0 nt sc1
	v_lshlrev_b32_e32 v2, 3, v0
	v_and_b32_e32 v1, 0x1f8, v2
	v_lshrrev_b32_e32 v32, 6, v0
	s_movk_i32 s6, 0x220
	s_waitcnt vmcnt(31)
	v_cvt_pk_bf16_f32 v4, v4, v5
	v_cvt_pk_bf16_f32 v5, v6, v7
	v_mad_u32_u24 v6, v32, s6, v1
	ds_write_b64 v6, v[4:5]
	v_add_u32_e32 v4, 0x200, v0
	v_lshrrev_b32_e32 v7, 6, v4
	s_waitcnt vmcnt(30)
	v_cvt_pk_bf16_f32 v4, v8, v9
	v_cvt_pk_bf16_f32 v5, v10, v11
	v_mad_u32_u24 v7, v7, s6, v1
	ds_write_b64 v7, v[4:5]
	s_waitcnt vmcnt(29)
	v_cvt_pk_bf16_f32 v4, v12, v13
	v_cvt_pk_bf16_f32 v5, v14, v15
	ds_write_b64 v6, v[4:5] offset:8704
	v_add_u32_e32 v4, 0x600, v0
	v_lshrrev_b32_e32 v7, 6, v4
	s_waitcnt vmcnt(28)
	v_cvt_pk_bf16_f32 v4, v16, v17
	v_cvt_pk_bf16_f32 v5, v18, v19
	v_mad_u32_u24 v7, v7, s6, v1
	ds_write_b64 v7, v[4:5]
	s_waitcnt vmcnt(27)
	v_cvt_pk_bf16_f32 v4, v20, v21
	v_cvt_pk_bf16_f32 v5, v22, v23
	ds_write_b64 v6, v[4:5] offset:17408
	v_add_u32_e32 v4, 0xa00, v0
	v_lshrrev_b32_e32 v7, 6, v4
	s_waitcnt vmcnt(26)
	v_cvt_pk_bf16_f32 v4, v24, v25
	v_cvt_pk_bf16_f32 v5, v26, v27
	v_mad_u32_u24 v7, v7, s6, v1
	ds_write_b64 v7, v[4:5]
	s_waitcnt vmcnt(25)
	v_cvt_pk_bf16_f32 v4, v28, v29
	v_cvt_pk_bf16_f32 v5, v30, v31
	ds_write_b64 v6, v[4:5] offset:26112
	v_add_u32_e32 v4, 0xe00, v0
	v_lshrrev_b32_e32 v7, 6, v4
	s_waitcnt vmcnt(24)
	v_cvt_pk_bf16_f32 v4, v98, v99
	v_cvt_pk_bf16_f32 v5, v100, v101
	v_mad_u32_u24 v7, v7, s6, v1
	ds_write_b64 v7, v[4:5]
	s_waitcnt vmcnt(23)
	v_cvt_pk_bf16_f32 v4, v102, v103
	v_cvt_pk_bf16_f32 v5, v104, v105
	ds_write_b64 v6, v[4:5] offset:34816
	v_add_u32_e32 v4, 0x1200, v0
	v_lshrrev_b32_e32 v7, 6, v4
	s_waitcnt vmcnt(22)
	v_cvt_pk_bf16_f32 v4, v106, v107
	v_cvt_pk_bf16_f32 v5, v108, v109
	v_mad_u32_u24 v7, v7, s6, v1
	ds_write_b64 v7, v[4:5]
	s_waitcnt vmcnt(21)
	v_cvt_pk_bf16_f32 v4, v110, v111
	v_cvt_pk_bf16_f32 v5, v112, v113
	ds_write_b64 v6, v[4:5] offset:43520
	v_add_u32_e32 v4, 0x1600, v0
	v_lshrrev_b32_e32 v7, 6, v4
	s_waitcnt vmcnt(20)
	v_cvt_pk_bf16_f32 v4, v114, v115
	v_cvt_pk_bf16_f32 v5, v116, v117
	v_mad_u32_u24 v7, v7, s6, v1
	ds_write_b64 v7, v[4:5]
	s_waitcnt vmcnt(19)
	v_cvt_pk_bf16_f32 v4, v118, v119
	v_cvt_pk_bf16_f32 v5, v120, v121
	ds_write_b64 v6, v[4:5] offset:52224
	v_add_u32_e32 v4, 0x1a00, v0
	v_lshrrev_b32_e32 v7, 6, v4
	s_waitcnt vmcnt(18)
	v_cvt_pk_bf16_f32 v4, v122, v123
	v_cvt_pk_bf16_f32 v5, v124, v125
	v_mad_u32_u24 v7, v7, s6, v1
	ds_write_b64 v7, v[4:5]
	s_waitcnt vmcnt(17)
	v_cvt_pk_bf16_f32 v4, v126, v127
	v_cvt_pk_bf16_f32 v5, v128, v129
	ds_write_b64 v6, v[4:5] offset:60928
	v_add_u32_e32 v4, 0x1e00, v0
	v_lshrrev_b32_e32 v6, 6, v4
	s_waitcnt vmcnt(16)
	v_cvt_pk_bf16_f32 v4, v132, v133
	v_cvt_pk_bf16_f32 v5, v134, v135
	v_mad_u32_u24 v1, v6, s6, v1
	ds_write_b64 v1, v[4:5]
	s_and_saveexec_b64 s[6:7], s[10:11]
	s_cbranch_execz .LBB0_4
	s_load_dwordx4 s[24:27], s[0:1], 0x10
	v_mov_b32_e32 v1, v3
	v_lshlrev_b64 v[4:5], 2, v[0:1]
	s_waitcnt lgkmcnt(0)
	v_lshl_add_u64 v[6:7], s[24:25], 0, v[4:5]
	global_load_dword v1, v[6:7], off
	v_lshl_add_u64 v[4:5], s[26:27], 0, v[4:5]
	global_load_dword v4, v[4:5], off
	v_add_u32_e32 v5, 0x22000, v130
	v_add_u32_e32 v6, 0x22200, v130
	s_waitcnt vmcnt(1)
	v_mul_f32_e32 v1, 0x4038aa3b, v1
	ds_write_b32 v5, v1
	s_waitcnt vmcnt(0)
	ds_write_b32 v6, v4
